# gemm1 K-loops: next tile's DMA global addresses advanced in the pre-barrier tail; only (m0 write, MFMA, LDS-DMA) between MFMAs
# baseline (speedup 1.0000x reference)
.LBB1_2:
	s_waitcnt vmcnt(9)
	s_waitcnt lgkmcnt(0)
	s_barrier
	s_lshl_b32 s28, s38, 15
	v_or_b32_e32 v53, s28, v50
	v_add_u32_e32 v88, s28, v92
	v_add_u32_e32 v53, v53, v52
	v_add_u32_e32 v89, s28, v93
	v_cndmask_b32_e64 v88, v88, v95, s[42:43]
	v_add_u32_e32 v95, 64, v95
	s_lshl_b32 s29, s37, 15
	s_add_u32 s30, s29, s41
	s_add_u32 s31, s29, s40
	ds_read_b128 v[100:103], v53
	ds_read_b128 v[104:107], v88 offset:16384
	v_mfma_f32_16x16x32_f16 v[14:17], v[62:65], v[58:61], v[14:17]
	ds_read_b128 v[108:111], v53 offset:1024
	v_mfma_f32_16x16x32_f16 v[30:33], v[54:57], v[58:61], v[30:33]
	ds_read_b128 v[112:115], v89 offset:16384
	v_mfma_f32_16x16x32_f16 v[22:25], v[54:57], v[66:69], v[22:25]
	ds_read_b128 v[116:119], v88 offset:18432
	v_mfma_f32_16x16x32_f16 v[6:9], v[62:65], v[66:69], v[6:9]
	ds_read_b128 v[120:123], v89 offset:18432
	v_mfma_f32_16x16x32_f16 v[26:29], v[54:57], v[70:73], v[26:29]
	ds_read_b128 v[124:127], v53 offset:8192
	v_mfma_f32_16x16x32_f16 v[30:33], v[80:83], v[58:61], v[30:33]
	ds_read_b128 v[128:131], v53 offset:9216
	s_mov_b32 m0, s30
	v_mfma_f32_16x16x32_f16 v[22:25], v[80:83], v[66:69], v[22:25]
	global_load_lds_dwordx4 v[40:41], off
	s_add_u32 m0, s30, 0x2000
	v_mfma_f32_16x16x32_f16 v[18:21], v[54:57], v[74:77], v[18:21]
	global_load_lds_dwordx4 v[38:39], off
	s_mov_b32 m0, s31
	v_mfma_f32_16x16x32_f16 v[14:17], v[84:87], v[58:61], v[14:17]
	global_load_lds_dwordx4 v[36:37], off
	v_mfma_f32_16x16x32_f16 v[10:13], v[62:65], v[70:73], v[10:13]
	v_mfma_f32_16x16x32_f16 v[6:9], v[84:87], v[66:69], v[6:9]
	v_mfma_f32_16x16x32_f16 v[2:5], v[62:65], v[74:77], v[2:5]
	v_lshl_add_u64 v[40:41], v[40:41], 0, 64
	v_lshl_add_u64 v[38:39], v[38:39], 0, 64
	v_lshl_add_u64 v[36:37], v[36:37], 0, 64
	s_add_i32 s36, s36, 1
	s_add_i32 s28, s37, 1
	s_cmp_lg_u32 s37, 4
	s_cselect_b32 s37, s28, 0
	s_add_i32 s28, s38, 1
	s_cmp_lg_u32 s38, 4
	s_cselect_b32 s38, s28, 0
	s_waitcnt vmcnt(9)
	s_waitcnt lgkmcnt(0)
	s_barrier
	s_lshl_b32 s28, s38, 15
	v_or_b32_e32 v53, s28, v50
	v_add_u32_e32 v88, s28, v92
	v_add_u32_e32 v53, v53, v52
	v_add_u32_e32 v89, s28, v93
	v_cndmask_b32_e64 v88, v88, v95, s[42:43]
	v_add_u32_e32 v95, 64, v95
	s_lshl_b32 s29, s37, 15
	s_add_u32 s30, s29, s41
	s_add_u32 s31, s29, s40
	ds_read_b128 v[54:57], v53
	ds_read_b128 v[58:61], v88 offset:16384
	v_mfma_f32_16x16x32_f16 v[14:17], v[108:111], v[104:107], v[14:17]
	ds_read_b128 v[62:65], v53 offset:1024
	v_mfma_f32_16x16x32_f16 v[30:33], v[100:103], v[104:107], v[30:33]
	ds_read_b128 v[66:69], v89 offset:16384
	v_mfma_f32_16x16x32_f16 v[22:25], v[100:103], v[112:115], v[22:25]
	ds_read_b128 v[70:73], v88 offset:18432
	v_mfma_f32_16x16x32_f16 v[6:9], v[108:111], v[112:115], v[6:9]
	ds_read_b128 v[74:77], v89 offset:18432
	v_mfma_f32_16x16x32_f16 v[26:29], v[100:103], v[116:119], v[26:29]
	ds_read_b128 v[80:83], v53 offset:8192
	v_mfma_f32_16x16x32_f16 v[30:33], v[124:127], v[104:107], v[30:33]
	ds_read_b128 v[84:87], v53 offset:9216
	s_mov_b32 m0, s30
	v_mfma_f32_16x16x32_f16 v[22:25], v[124:127], v[112:115], v[22:25]
	global_load_lds_dwordx4 v[40:41], off
	s_add_u32 m0, s30, 0x2000
	v_mfma_f32_16x16x32_f16 v[18:21], v[100:103], v[120:123], v[18:21]
	global_load_lds_dwordx4 v[38:39], off
	s_mov_b32 m0, s31
	v_mfma_f32_16x16x32_f16 v[14:17], v[128:131], v[104:107], v[14:17]
	global_load_lds_dwordx4 v[36:37], off
	v_mfma_f32_16x16x32_f16 v[10:13], v[108:111], v[116:119], v[10:13]
	v_mfma_f32_16x16x32_f16 v[6:9], v[128:131], v[112:115], v[6:9]
	v_mfma_f32_16x16x32_f16 v[2:5], v[108:111], v[120:123], v[2:5]
	v_lshl_add_u64 v[40:41], v[40:41], 0, 64
	v_lshl_add_u64 v[38:39], v[38:39], 0, 64
	v_lshl_add_u64 v[36:37], v[36:37], 0, 64
	s_add_i32 s36, s36, 1
	s_add_i32 s28, s37, 1
	s_cmp_lg_u32 s37, 4
	s_cselect_b32 s37, s28, 0
	s_add_i32 s28, s38, 1
	s_cmp_lg_u32 s38, 4
	s_cselect_b32 s38, s28, 0
	s_cmp_lt_u32 s36, 26
	s_cbranch_scc1 .LBB1_2
	s_waitcnt vmcnt(9)
	s_waitcnt lgkmcnt(0)
	s_barrier
	s_lshl_b32 s28, s38, 15
	v_or_b32_e32 v53, s28, v50
	v_add_u32_e32 v88, s28, v92
	v_add_u32_e32 v53, v53, v52
	v_add_u32_e32 v89, s28, v93
	v_cndmask_b32_e64 v88, v88, v95, s[42:43]
	v_add_u32_e32 v95, 64, v95
	s_lshl_b32 s29, s37, 15
	s_add_u32 s30, s29, s41
	s_add_u32 s31, s29, s40
	ds_read_b128 v[100:103], v53
	ds_read_b128 v[104:107], v88 offset:16384
	v_mfma_f32_16x16x32_f16 v[14:17], v[62:65], v[58:61], v[14:17]
	ds_read_b128 v[108:111], v53 offset:1024
	v_mfma_f32_16x16x32_f16 v[30:33], v[54:57], v[58:61], v[30:33]
	ds_read_b128 v[112:115], v89 offset:16384
	v_mfma_f32_16x16x32_f16 v[22:25], v[54:57], v[66:69], v[22:25]
	ds_read_b128 v[116:119], v88 offset:18432
	v_mfma_f32_16x16x32_f16 v[6:9], v[62:65], v[66:69], v[6:9]
	ds_read_b128 v[120:123], v89 offset:18432
	v_mfma_f32_16x16x32_f16 v[26:29], v[54:57], v[70:73], v[26:29]
	ds_read_b128 v[124:127], v53 offset:8192
	v_mfma_f32_16x16x32_f16 v[30:33], v[80:83], v[58:61], v[30:33]
	ds_read_b128 v[128:131], v53 offset:9216
	s_mov_b32 m0, s30
	v_mfma_f32_16x16x32_f16 v[22:25], v[80:83], v[66:69], v[22:25]
	global_load_lds_dwordx4 v[40:41], off
	s_add_u32 m0, s30, 0x2000
	v_mfma_f32_16x16x32_f16 v[18:21], v[54:57], v[74:77], v[18:21]
	global_load_lds_dwordx4 v[38:39], off
	s_mov_b32 m0, s31
	v_mfma_f32_16x16x32_f16 v[14:17], v[84:87], v[58:61], v[14:17]
	global_load_lds_dwordx4 v[36:37], off
	v_mfma_f32_16x16x32_f16 v[10:13], v[62:65], v[70:73], v[10:13]
	v_mfma_f32_16x16x32_f16 v[6:9], v[84:87], v[66:69], v[6:9]
	v_mfma_f32_16x16x32_f16 v[2:5], v[62:65], v[74:77], v[2:5]
	v_lshl_add_u64 v[40:41], v[40:41], 0, 64
	v_lshl_add_u64 v[38:39], v[38:39], 0, 64
	v_lshl_add_u64 v[36:37], v[36:37], 0, 64
	s_add_i32 s36, s36, 1
	s_add_i32 s28, s37, 1
	s_cmp_lg_u32 s37, 4
	s_cselect_b32 s37, s28, 0
	s_add_i32 s28, s38, 1
	s_cmp_lg_u32 s38, 4
	s_cselect_b32 s38, s28, 0
	s_waitcnt vmcnt(9)
	s_waitcnt lgkmcnt(0)
	s_barrier
	s_lshl_b32 s28, s38, 15
	v_or_b32_e32 v53, s28, v50
	v_add_u32_e32 v88, s28, v92
	v_add_u32_e32 v53, v53, v52
	v_add_u32_e32 v89, s28, v93
	v_cndmask_b32_e64 v88, v88, v95, s[42:43]
	v_add_u32_e32 v95, 64, v95
	ds_read_b128 v[54:57], v53
	ds_read_b128 v[58:61], v88 offset:16384
	v_mfma_f32_16x16x32_f16 v[14:17], v[108:111], v[104:107], v[14:17]
	ds_read_b128 v[62:65], v53 offset:1024
	v_mfma_f32_16x16x32_f16 v[30:33], v[100:103], v[104:107], v[30:33]
	ds_read_b128 v[66:69], v89 offset:16384
	v_mfma_f32_16x16x32_f16 v[22:25], v[100:103], v[112:115], v[22:25]
	ds_read_b128 v[70:73], v88 offset:18432
	v_mfma_f32_16x16x32_f16 v[6:9], v[108:111], v[112:115], v[6:9]
	ds_read_b128 v[74:77], v89 offset:18432
	v_mfma_f32_16x16x32_f16 v[26:29], v[100:103], v[116:119], v[26:29]
	ds_read_b128 v[80:83], v53 offset:8192
	v_mfma_f32_16x16x32_f16 v[30:33], v[124:127], v[104:107], v[30:33]
	ds_read_b128 v[84:87], v53 offset:9216
	v_mfma_f32_16x16x32_f16 v[22:25], v[124:127], v[112:115], v[22:25]
	v_mfma_f32_16x16x32_f16 v[18:21], v[100:103], v[120:123], v[18:21]
	v_mfma_f32_16x16x32_f16 v[14:17], v[128:131], v[104:107], v[14:17]
	v_mfma_f32_16x16x32_f16 v[10:13], v[108:111], v[116:119], v[10:13]
	v_mfma_f32_16x16x32_f16 v[6:9], v[128:131], v[112:115], v[6:9]
	v_mfma_f32_16x16x32_f16 v[2:5], v[108:111], v[120:123], v[2:5]
	s_add_i32 s36, s36, 1
	s_add_i32 s28, s37, 1
	s_cmp_lg_u32 s37, 4
	s_cselect_b32 s37, s28, 0
	s_add_i32 s28, s38, 1
	s_cmp_lg_u32 s38, 4
	s_cselect_b32 s38, s28, 0
	s_waitcnt vmcnt(6)
	s_waitcnt lgkmcnt(0)
	s_barrier
	s_lshl_b32 s28, s38, 15
	v_or_b32_e32 v53, s28, v50
	v_add_u32_e32 v88, s28, v92
	v_add_u32_e32 v53, v53, v52
	v_add_u32_e32 v89, s28, v93
	v_cndmask_b32_e64 v88, v88, v95, s[42:43]
	v_add_u32_e32 v95, 64, v95
	ds_read_b128 v[100:103], v53
	ds_read_b128 v[104:107], v88 offset:16384
	v_mfma_f32_16x16x32_f16 v[14:17], v[62:65], v[58:61], v[14:17]
	ds_read_b128 v[108:111], v53 offset:1024
	v_mfma_f32_16x16x32_f16 v[30:33], v[54:57], v[58:61], v[30:33]
	ds_read_b128 v[112:115], v89 offset:16384
	v_mfma_f32_16x16x32_f16 v[22:25], v[54:57], v[66:69], v[22:25]
	ds_read_b128 v[116:119], v88 offset:18432
	v_mfma_f32_16x16x32_f16 v[6:9], v[62:65], v[66:69], v[6:9]
	ds_read_b128 v[120:123], v89 offset:18432
	v_mfma_f32_16x16x32_f16 v[26:29], v[54:57], v[70:73], v[26:29]
	ds_read_b128 v[124:127], v53 offset:8192
	v_mfma_f32_16x16x32_f16 v[30:33], v[80:83], v[58:61], v[30:33]
	ds_read_b128 v[128:131], v53 offset:9216
	v_mfma_f32_16x16x32_f16 v[22:25], v[80:83], v[66:69], v[22:25]
	v_mfma_f32_16x16x32_f16 v[18:21], v[54:57], v[74:77], v[18:21]
	v_mfma_f32_16x16x32_f16 v[14:17], v[84:87], v[58:61], v[14:17]
	v_mfma_f32_16x16x32_f16 v[10:13], v[62:65], v[70:73], v[10:13]
	v_mfma_f32_16x16x32_f16 v[6:9], v[84:87], v[66:69], v[6:9]
	v_mfma_f32_16x16x32_f16 v[2:5], v[62:65], v[74:77], v[2:5]
	s_add_i32 s36, s36, 1
	s_add_i32 s28, s37, 1
	s_cmp_lg_u32 s37, 4
	s_cselect_b32 s37, s28, 0
	s_add_i32 s28, s38, 1
	s_cmp_lg_u32 s38, 4
	s_cselect_b32 s38, s28, 0
	s_waitcnt vmcnt(3)
	s_waitcnt lgkmcnt(0)
	s_barrier
	s_lshl_b32 s28, s38, 15
	v_or_b32_e32 v53, s28, v50
	v_add_u32_e32 v88, s28, v92
	v_add_u32_e32 v53, v53, v52
	v_add_u32_e32 v89, s28, v93
	v_cndmask_b32_e64 v88, v88, v95, s[42:43]
	v_add_u32_e32 v95, 64, v95
	ds_read_b128 v[54:57], v53
	ds_read_b128 v[58:61], v88 offset:16384
	v_mfma_f32_16x16x32_f16 v[14:17], v[108:111], v[104:107], v[14:17]
	ds_read_b128 v[62:65], v53 offset:1024
	v_mfma_f32_16x16x32_f16 v[30:33], v[100:103], v[104:107], v[30:33]
	ds_read_b128 v[66:69], v89 offset:16384
	v_mfma_f32_16x16x32_f16 v[22:25], v[100:103], v[112:115], v[22:25]
	ds_read_b128 v[70:73], v88 offset:18432
	v_mfma_f32_16x16x32_f16 v[6:9], v[108:111], v[112:115], v[6:9]
	ds_read_b128 v[74:77], v89 offset:18432
	v_mfma_f32_16x16x32_f16 v[26:29], v[100:103], v[116:119], v[26:29]
	ds_read_b128 v[80:83], v53 offset:8192
	v_mfma_f32_16x16x32_f16 v[30:33], v[124:127], v[104:107], v[30:33]
	ds_read_b128 v[84:87], v53 offset:9216
	v_mfma_f32_16x16x32_f16 v[22:25], v[124:127], v[112:115], v[22:25]
	v_mfma_f32_16x16x32_f16 v[18:21], v[100:103], v[120:123], v[18:21]
	v_mfma_f32_16x16x32_f16 v[14:17], v[128:131], v[104:107], v[14:17]
	v_mfma_f32_16x16x32_f16 v[10:13], v[108:111], v[116:119], v[10:13]
	v_mfma_f32_16x16x32_f16 v[6:9], v[128:131], v[112:115], v[6:9]
	v_mfma_f32_16x16x32_f16 v[2:5], v[108:111], v[120:123], v[2:5]
	s_add_i32 s36, s36, 1
	s_add_i32 s28, s37, 1
	s_cmp_lg_u32 s37, 4
	s_cselect_b32 s37, s28, 0
	s_add_i32 s28, s38, 1
	s_cmp_lg_u32 s38, 4
	s_cselect_b32 s38, s28, 0
	s_waitcnt vmcnt(0)
	s_waitcnt lgkmcnt(0)
	s_barrier
	s_lshl_b32 s28, s38, 15
	v_or_b32_e32 v53, s28, v50
	v_add_u32_e32 v88, s28, v92
	v_add_u32_e32 v53, v53, v52
	v_add_u32_e32 v89, s28, v93
	v_cndmask_b32_e64 v88, v88, v95, s[42:43]
	v_add_u32_e32 v95, 64, v95
	ds_read_b128 v[100:103], v53
	ds_read_b128 v[104:107], v88 offset:16384
	v_mfma_f32_16x16x32_f16 v[14:17], v[62:65], v[58:61], v[14:17]
	ds_read_b128 v[108:111], v53 offset:1024
	v_mfma_f32_16x16x32_f16 v[30:33], v[54:57], v[58:61], v[30:33]
	ds_read_b128 v[112:115], v89 offset:16384
	v_mfma_f32_16x16x32_f16 v[22:25], v[54:57], v[66:69], v[22:25]
	ds_read_b128 v[116:119], v88 offset:18432
	v_mfma_f32_16x16x32_f16 v[6:9], v[62:65], v[66:69], v[6:9]
	ds_read_b128 v[120:123], v89 offset:18432
	v_mfma_f32_16x16x32_f16 v[26:29], v[54:57], v[70:73], v[26:29]
	ds_read_b128 v[124:127], v53 offset:8192
	v_mfma_f32_16x16x32_f16 v[30:33], v[80:83], v[58:61], v[30:33]
	ds_read_b128 v[128:131], v53 offset:9216
	v_mfma_f32_16x16x32_f16 v[22:25], v[80:83], v[66:69], v[22:25]
	v_mfma_f32_16x16x32_f16 v[18:21], v[54:57], v[74:77], v[18:21]
	v_mfma_f32_16x16x32_f16 v[14:17], v[84:87], v[58:61], v[14:17]
	v_mfma_f32_16x16x32_f16 v[10:13], v[62:65], v[70:73], v[10:13]
	v_mfma_f32_16x16x32_f16 v[6:9], v[84:87], v[66:69], v[6:9]
	v_mfma_f32_16x16x32_f16 v[2:5], v[62:65], v[74:77], v[2:5]
	s_add_i32 s36, s36, 1
	s_add_i32 s28, s37, 1
	s_cmp_lg_u32 s37, 4
	s_cselect_b32 s37, s28, 0
	s_add_i32 s28, s38, 1
	s_cmp_lg_u32 s38, 4
	s_cselect_b32 s38, s28, 0
	s_waitcnt lgkmcnt(0)
	v_mfma_f32_16x16x32_f16 v[14:17], v[108:111], v[104:107], v[14:17]
	v_mfma_f32_16x16x32_f16 v[30:33], v[100:103], v[104:107], v[30:33]
	v_mfma_f32_16x16x32_f16 v[22:25], v[100:103], v[112:115], v[22:25]
	v_mfma_f32_16x16x32_f16 v[6:9], v[108:111], v[112:115], v[6:9]
	v_mfma_f32_16x16x32_f16 v[26:29], v[100:103], v[116:119], v[26:29]
	v_mfma_f32_16x16x32_f16 v[30:33], v[124:127], v[104:107], v[30:33]
	v_mfma_f32_16x16x32_f16 v[22:25], v[124:127], v[112:115], v[22:25]
	v_mfma_f32_16x16x32_f16 v[18:21], v[100:103], v[120:123], v[18:21]
	v_mfma_f32_16x16x32_f16 v[14:17], v[128:131], v[104:107], v[14:17]
	v_mfma_f32_16x16x32_f16 v[10:13], v[108:111], v[116:119], v[10:13]
	v_mfma_f32_16x16x32_f16 v[6:9], v[128:131], v[112:115], v[6:9]
	v_mfma_f32_16x16x32_f16 v[2:5], v[108:111], v[120:123], v[2:5]
	s_nop 1

.Lqk_bias_done:
	v_lshlrev_b32_e32 v5, 7, v0
	v_lshlrev_b32_e32 v2, 3, v2
	s_mov_b32 s7, 0x1fc00
	v_mov_b32_e32 v6, 0x10000
	s_add_u32 s16, s24, s18
	v_and_b32_e32 v3, 56, v2
	v_and_b32_e32 v4, 0xfc00, v5
	v_bitop3_b32 v5, v5, s7, v6 bitop3:0xc8
	v_lshlrev_b32_e32 v8, 8, v0
	s_mov_b32 s7, 0x3f800
	v_mov_b32_e32 v7, 0x20000
	s_addc_u32 s17, s25, s19
	v_or_b32_e32 v2, v4, v3
	v_bitop3_b32 v7, v8, s7, v7 bitop3:0xc8
	s_mov_b32 s7, 0x7f800
	v_mov_b32_e32 v11, 0x60000
	s_waitcnt lgkmcnt(0)
	s_add_u32 s22, s0, s2
	v_and_b32_e32 v6, 0x1f800, v8
	v_bitop3_b32 v8, v8, s7, v11 bitop3:0xc8
	v_lshlrev_b32_e32 v12, 1, v2
	v_mov_b32_e32 v2, 0
	v_readfirstlane_b32 s7, v79
	v_or_b32_e32 v9, v5, v3
	s_addc_u32 s23, s1, s3
	v_mov_b32_e32 v13, v2
	s_mov_b32 m0, s7
	v_lshl_add_u64 v[14:15], s[22:23], 0, v[12:13]
	global_load_lds_dwordx4 v12, s[22:23]
	v_lshlrev_b32_e32 v12, 1, v9
	v_or_b32_e32 v9, 0x2000, v79
	v_or_b32_e32 v10, v6, v3
	v_readfirstlane_b32 s7, v9
	v_or_b32_e32 v9, 0x4000, v79
	s_mov_b32 m0, s7
	v_readfirstlane_b32 s7, v9
	v_or_b32_e32 v9, 0x6000, v79
	v_or_b32_e32 v18, v7, v3
	v_lshlrev_b32_e32 v10, 1, v10
	global_load_lds_dwordx4 v12, s[22:23]
	s_mov_b32 m0, s7
	v_readfirstlane_b32 s7, v9
	v_or_b32_e32 v9, 0x8000, v79
	v_mov_b32_e32 v11, v2
	global_load_lds_dwordx4 v10, s[16:17]
	v_lshlrev_b32_e32 v18, 1, v18
	s_mov_b32 m0, s7
	v_readfirstlane_b32 s7, v9
	v_or_b32_e32 v9, 0xa000, v79
	v_or_b32_e32 v22, v8, v3
	v_lshl_add_u64 v[16:17], s[22:23], 0, v[12:13]
	v_lshl_add_u64 v[12:13], s[16:17], 0, v[10:11]
	v_mov_b32_e32 v19, v2
	global_load_lds_dwordx4 v18, s[16:17]
	v_or_b32_e32 v10, 0x80000, v10
	s_mov_b32 m0, s7
	v_readfirstlane_b32 s7, v9
	v_lshl_add_u64 v[20:21], s[16:17], 0, v[18:19]
	v_lshl_add_u64 v[18:19], s[16:17], 0, v[10:11]
	global_load_lds_dwordx4 v10, s[16:17]
	v_lshlrev_b32_e32 v10, 1, v22
	s_mov_b32 m0, s7
	v_or_b32_e32 v9, 0xc000, v79
	v_lshl_add_u64 v[22:23], s[16:17], 0, v[10:11]
	global_load_lds_dwordx4 v10, s[16:17]
	s_mov_b64 s[16:17], 0x80
	v_readfirstlane_b32 s7, v9
	v_or_b32_e32 v9, 0xe000, v79
	v_lshl_add_u64 v[10:11], v[14:15], 0, s[16:17]
	s_mov_b32 m0, s7
	v_readfirstlane_b32 s7, v9
	v_or_b32_e32 v9, 0x10000, v79
	global_load_lds_dwordx4 v[10:11], off
	v_lshl_add_u64 v[10:11], v[16:17], 0, s[16:17]
	s_mov_b32 m0, s7
	v_readfirstlane_b32 s7, v9
	v_or_b32_e32 v9, 0x12000, v79
	global_load_lds_dwordx4 v[10:11], off
	v_lshl_add_u64 v[10:11], v[12:13], 0, s[16:17]
	s_mov_b32 m0, s7
	v_readfirstlane_b32 s7, v9
	v_or_b32_e32 v9, 0x14000, v79
	global_load_lds_dwordx4 v[10:11], off
	v_lshl_add_u64 v[10:11], v[20:21], 0, s[16:17]
	s_mov_b32 m0, s7
	v_readfirstlane_b32 s7, v9
	v_or_b32_e32 v9, 0x16000, v79
	global_load_lds_dwordx4 v[10:11], off
	v_lshl_add_u64 v[10:11], v[18:19], 0, s[16:17]
	s_mov_b32 m0, s7
	v_readfirstlane_b32 s7, v9
	global_load_lds_dwordx4 v[10:11], off
	v_lshl_add_u64 v[10:11], v[22:23], 0, s[16:17]
	s_mov_b32 m0, s7
	s_nop 0
	global_load_lds_dwordx4 v[10:11], off
	s_cmp_lt_i32 s20, 16
	s_cselect_b64 s[16:17], -1, 0
	s_cmp_gt_i32 s20, 15
	v_bfe_u32 v9, v0, 6, 2
	s_cselect_b64 vcc, -1, 0
	v_cndmask_b32_e32 v83, v78, v9, vcc
	v_cndmask_b32_e32 v9, v9, v78, vcc
	s_and_b64 s[22:23], vcc, exec
	v_lshl_or_b32 v80, v9, 6, v42
	v_bfe_u32 v9, v0, 1, 3
	s_cselect_b32 s26, 0x2000, 0
	s_cselect_b32 s27, 0, 0x2000
	v_bitop3_b32 v9, v1, v9, 4 bitop3:0x36
	s_add_u32 s18, s24, s18
	v_lshlrev_b32_e32 v84, 4, v9
	v_add_lshl_u32 v8, v8, v3, 1
	v_mov_b32_e32 v9, v2
	s_addc_u32 s19, s25, s19
	v_lshl_add_u64 v[8:9], s[18:19], 0, v[8:9]
	s_mov_b64 s[22:23], 0x100
	v_lshl_add_u64 v[66:67], v[8:9], 0, s[22:23]
	v_add_lshl_u32 v8, v7, v3, 1
	v_mov_b32_e32 v9, v2
	v_lshl_add_u64 v[8:9], s[18:19], 0, v[8:9]
	v_add_lshl_u32 v6, v6, v3, 1
	v_mov_b32_e32 v7, v2
	v_lshl_add_u64 v[68:69], v[8:9], 0, s[22:23]
	v_lshl_add_u64 v[8:9], s[18:19], 0, v[6:7]
	v_or_b32_e32 v6, 0x80000, v6
	v_lshlrev_b32_e32 v82, 6, v83
	v_lshl_add_u64 v[6:7], s[18:19], 0, v[6:7]
	s_add_u32 s0, s0, s2
	v_or_b32_e32 v10, v82, v42
	v_lshl_add_u64 v[72:73], v[6:7], 0, s[22:23]
	v_add_lshl_u32 v6, v5, v3, 1
	v_mov_b32_e32 v7, v2
	s_addc_u32 s1, s1, s3
	v_add_lshl_u32 v4, v4, v3, 1
	v_mov_b32_e32 v5, v2
	v_lshlrev_b32_e32 v86, 7, v10
	v_bitop3_b32 v10, v43, v1, 7 bitop3:0x6c
	v_lshl_add_u64 v[6:7], s[0:1], 0, v[6:7]
	v_lshl_add_u64 v[4:5], s[0:1], 0, v[4:5]
	v_lshlrev_b32_e32 v85, 4, v10
	v_lshlrev_b32_e32 v81, 7, v80
	v_lshl_add_u64 v[70:71], v[8:9], 0, s[22:23]
	v_lshl_add_u64 v[74:75], v[6:7], 0, s[22:23]
	v_lshl_add_u64 v[76:77], v[4:5], 0, s[22:23]
	s_mov_b32 s18, 2
	s_mov_b64 s[0:1], 0
	s_lshl_b32 s3, s26, 1
	s_lshl_b32 s2, s27, 1
	v_mov_b32_e32 v3, v2
	v_mov_b32_e32 v4, v2
	v_mov_b32_e32 v5, v2
	v_mov_b32_e32 v6, v2
	v_mov_b32_e32 v7, v2
	v_mov_b32_e32 v8, v2
	v_mov_b32_e32 v9, v2
	v_mov_b32_e32 v10, v2
	v_mov_b32_e32 v11, v2
	v_mov_b32_e32 v12, v2
	v_mov_b32_e32 v13, v2
	v_mov_b32_e32 v14, v2
	v_mov_b32_e32 v15, v2
	v_mov_b32_e32 v16, v2
	v_mov_b32_e32 v17, v2
	v_mov_b32_e32 v18, v2
	v_mov_b32_e32 v19, v2
	v_mov_b32_e32 v20, v2
	v_mov_b32_e32 v21, v2
	v_mov_b32_e32 v22, v2
	v_mov_b32_e32 v23, v2
	v_mov_b32_e32 v24, v2
	v_mov_b32_e32 v25, v2
	v_mov_b32_e32 v26, v2
	v_mov_b32_e32 v27, v2
	v_mov_b32_e32 v28, v2
	v_mov_b32_e32 v29, v2
	v_mov_b32_e32 v30, v2
	v_mov_b32_e32 v31, v2
	v_mov_b32_e32 v32, v2
	v_mov_b32_e32 v33, v2
	v_mov_b32_e32 v34, v2
	v_mov_b32_e32 v35, v2
	v_mov_b32_e32 v36, v2
	v_mov_b32_e32 v37, v2
	v_mov_b32_e32 v38, v2
	v_mov_b32_e32 v39, v2
	v_mov_b32_e32 v40, v2
	v_mov_b32_e32 v41, v2
	v_mov_b32_e32 v42, v2
	v_mov_b32_e32 v43, v2
	v_mov_b32_e32 v44, v2
	v_mov_b32_e32 v45, v2
	v_mov_b32_e32 v46, v2
	v_mov_b32_e32 v47, v2
	v_mov_b32_e32 v48, v2
	v_mov_b32_e32 v49, v2
	v_mov_b32_e32 v50, v2
	v_mov_b32_e32 v51, v2
	v_mov_b32_e32 v52, v2
	v_mov_b32_e32 v53, v2
	v_mov_b32_e32 v54, v2
	v_mov_b32_e32 v55, v2
	v_mov_b32_e32 v56, v2
	v_mov_b32_e32 v57, v2
	v_mov_b32_e32 v58, v2
	v_mov_b32_e32 v59, v2
	v_mov_b32_e32 v60, v2
	v_mov_b32_e32 v61, v2
	v_mov_b32_e32 v62, v2
	v_mov_b32_e32 v63, v2
	v_mov_b32_e32 v64, v2
	v_mov_b32_e32 v65, v2
	v_readfirstlane_b32 s44, v79
	s_mov_b32 s45, 0
	s_mov_b32 s46, 1
	s_mov_b32 s48, 0
	s_mov_b64 s[0:1], 0
	s_add_u32 s49, s44, 0x18000
	s_mov_b32 m0, s49
	s_nop 0
	global_load_lds_dwordx4 v[76:77], off
	s_add_u32 m0, s49, 0x2000
	s_nop 0
	global_load_lds_dwordx4 v[74:75], off
	s_add_u32 m0, s49, 0x4000
	s_nop 0
	global_load_lds_dwordx4 v[70:71], off
	s_add_u32 m0, s49, 0x6000
	s_nop 0
	global_load_lds_dwordx4 v[68:69], off
	s_add_u32 m0, s49, 0x8000
	s_nop 0
	global_load_lds_dwordx4 v[72:73], off
	s_add_u32 m0, s49, 0xa000
	s_nop 0
	global_load_lds_dwordx4 v[66:67], off
	s_mov_b64 s[0:1], 0x80
	v_lshl_add_u64 v[76:77], v[76:77], 0, s[0:1]
	v_lshl_add_u64 v[74:75], v[74:75], 0, s[0:1]
	v_lshl_add_u64 v[70:71], v[70:71], 0, s[0:1]
	v_lshl_add_u64 v[68:69], v[68:69], 0, s[0:1]
	v_lshl_add_u64 v[72:73], v[72:73], 0, s[0:1]
	v_lshl_add_u64 v[66:67], v[66:67], 0, s[0:1]
	s_waitcnt vmcnt(12)
	s_barrier
	s_mov_b32 s46, 0
	s_mul_i32 s49, s46, 0xc000
	s_add_u32 s50, s49, s3
	s_add_u32 s51, s49, s2
	v_add3_u32 v120, s50, v86, v85
	v_add3_u32 v121, s50, v86, v84
	v_add3_u32 v122, s51, v81, v85
	v_add3_u32 v123, s51, v81, v84
	ds_read_b128 v[88:91], v120
	ds_read_b128 v[92:95], v120 offset:2048
	ds_read_b128 v[96:99], v120 offset:4096
	ds_read_b128 v[100:103], v120 offset:6144
	ds_read_b128 v[104:107], v122
	ds_read_b128 v[108:111], v122 offset:2048
	ds_read_b128 v[112:115], v122 offset:4096
	ds_read_b128 v[116:119], v122 offset:6144
	ds_read_b128 v[144:147], v121
	ds_read_b128 v[148:151], v121 offset:2048
	ds_read_b128 v[152:155], v121 offset:4096
	ds_read_b128 v[156:159], v121 offset:6144
	ds_read_b128 v[160:163], v123
	ds_read_b128 v[164:167], v123 offset:2048
	ds_read_b128 v[168:171], v123 offset:4096
	ds_read_b128 v[172:175], v123 offset:6144
	s_mov_b32 s46, 1
.LBB1_36:
	s_waitcnt vmcnt(6)
	s_waitcnt lgkmcnt(0)
	s_barrier
	s_mul_i32 s49, s46, 0xc000
	s_add_u32 s50, s49, s3
	s_add_u32 s51, s49, s2
	v_add3_u32 v120, s50, v86, v85
	v_add3_u32 v121, s50, v86, v84
	v_add3_u32 v122, s51, v81, v85
	v_add3_u32 v123, s51, v81, v84
	s_mul_i32 s49, s45, 0xc000
	s_add_u32 s49, s49, s44
	s_setprio 1
	ds_read_b128 v[176:179], v120
	ds_read_b128 v[180:183], v120 offset:2048
	ds_read_b128 v[184:187], v120 offset:4096
	ds_read_b128 v[188:191], v120 offset:6144
	v_mfma_f32_16x16x32_f16 v[62:65], v[88:91], v[104:107], v[62:65]
	ds_read_b128 v[192:195], v122
	v_mfma_f32_16x16x32_f16 v[58:61], v[88:91], v[108:111], v[58:61]
	ds_read_b128 v[196:199], v122 offset:2048
	v_mfma_f32_16x16x32_f16 v[54:57], v[88:91], v[112:115], v[54:57]
	ds_read_b128 v[200:203], v122 offset:4096
	v_mfma_f32_16x16x32_f16 v[50:53], v[88:91], v[116:119], v[50:53]
	ds_read_b128 v[204:207], v122 offset:6144
	v_mfma_f32_16x16x32_f16 v[46:49], v[92:95], v[104:107], v[46:49]
	ds_read_b128 v[208:211], v121
	v_mfma_f32_16x16x32_f16 v[42:45], v[92:95], v[108:111], v[42:45]
	ds_read_b128 v[212:215], v121 offset:2048
	v_mfma_f32_16x16x32_f16 v[38:41], v[92:95], v[112:115], v[38:41]
	ds_read_b128 v[216:219], v121 offset:4096
	v_mfma_f32_16x16x32_f16 v[34:37], v[92:95], v[116:119], v[34:37]
	ds_read_b128 v[220:223], v121 offset:6144
	v_mfma_f32_16x16x32_f16 v[30:33], v[96:99], v[104:107], v[30:33]
	ds_read_b128 v[224:227], v123
	v_mfma_f32_16x16x32_f16 v[26:29], v[96:99], v[108:111], v[26:29]
	ds_read_b128 v[228:231], v123 offset:2048
	v_mfma_f32_16x16x32_f16 v[22:25], v[96:99], v[112:115], v[22:25]
	ds_read_b128 v[232:235], v123 offset:4096
	v_mfma_f32_16x16x32_f16 v[18:21], v[96:99], v[116:119], v[18:21]
	ds_read_b128 v[236:239], v123 offset:6144
	v_mfma_f32_16x16x32_f16 v[14:17], v[100:103], v[104:107], v[14:17]
	v_mfma_f32_16x16x32_f16 v[10:13], v[100:103], v[108:111], v[10:13]
	s_mov_b32 m0, s49
	v_mfma_f32_16x16x32_f16 v[6:9], v[100:103], v[112:115], v[6:9]
	global_load_lds_dwordx4 v[76:77], off
	v_mfma_f32_16x16x32_f16 v[2:5], v[100:103], v[116:119], v[2:5]
	v_mfma_f32_16x16x32_f16 v[62:65], v[144:147], v[160:163], v[62:65]
	s_add_u32 m0, s49, 0x2000
	v_mfma_f32_16x16x32_f16 v[58:61], v[144:147], v[164:167], v[58:61]
	global_load_lds_dwordx4 v[74:75], off
	v_mfma_f32_16x16x32_f16 v[54:57], v[144:147], v[168:171], v[54:57]
	v_mfma_f32_16x16x32_f16 v[50:53], v[144:147], v[172:175], v[50:53]
	s_add_u32 m0, s49, 0x4000
	v_mfma_f32_16x16x32_f16 v[46:49], v[148:151], v[160:163], v[46:49]
	global_load_lds_dwordx4 v[70:71], off
	v_mfma_f32_16x16x32_f16 v[42:45], v[148:151], v[164:167], v[42:45]
	v_mfma_f32_16x16x32_f16 v[38:41], v[148:151], v[168:171], v[38:41]
	s_add_u32 m0, s49, 0x6000
	v_mfma_f32_16x16x32_f16 v[34:37], v[148:151], v[172:175], v[34:37]
	global_load_lds_dwordx4 v[68:69], off
	v_mfma_f32_16x16x32_f16 v[30:33], v[152:155], v[160:163], v[30:33]
	v_mfma_f32_16x16x32_f16 v[26:29], v[152:155], v[164:167], v[26:29]
	s_add_u32 m0, s49, 0x8000
	v_mfma_f32_16x16x32_f16 v[22:25], v[152:155], v[168:171], v[22:25]
	global_load_lds_dwordx4 v[72:73], off
	v_mfma_f32_16x16x32_f16 v[18:21], v[152:155], v[172:175], v[18:21]
	v_mfma_f32_16x16x32_f16 v[14:17], v[156:159], v[160:163], v[14:17]
	s_add_u32 m0, s49, 0xa000
	v_mfma_f32_16x16x32_f16 v[10:13], v[156:159], v[164:167], v[10:13]
	global_load_lds_dwordx4 v[66:67], off
	v_mfma_f32_16x16x32_f16 v[6:9], v[156:159], v[168:171], v[6:9]
	v_mfma_f32_16x16x32_f16 v[2:5], v[156:159], v[172:175], v[2:5]
	s_setprio 0
	v_lshl_add_u64 v[76:77], v[76:77], 0, s[0:1]
	v_lshl_add_u64 v[74:75], v[74:75], 0, s[0:1]
	v_lshl_add_u64 v[70:71], v[70:71], 0, s[0:1]
	v_lshl_add_u64 v[68:69], v[68:69], 0, s[0:1]
	v_lshl_add_u64 v[72:73], v[72:73], 0, s[0:1]
	v_lshl_add_u64 v[66:67], v[66:67], 0, s[0:1]
	s_add_i32 s48, s48, 1
	s_add_i32 s49, s45, 1
	s_cmp_lg_u32 s45, 2
	s_cselect_b32 s45, s49, 0
	s_add_i32 s49, s46, 1
	s_cmp_lg_u32 s46, 2
	s_cselect_b32 s46, s49, 0
	s_waitcnt vmcnt(6)
	s_waitcnt lgkmcnt(0)
	s_barrier
	s_mul_i32 s49, s46, 0xc000
	s_add_u32 s50, s49, s3
	s_add_u32 s51, s49, s2
	v_add3_u32 v120, s50, v86, v85
	v_add3_u32 v121, s50, v86, v84
	v_add3_u32 v122, s51, v81, v85
	v_add3_u32 v123, s51, v81, v84
	s_mul_i32 s49, s45, 0xc000
	s_add_u32 s49, s49, s44
	s_setprio 1
	ds_read_b128 v[88:91], v120
	ds_read_b128 v[92:95], v120 offset:2048
	ds_read_b128 v[96:99], v120 offset:4096
	ds_read_b128 v[100:103], v120 offset:6144
	v_mfma_f32_16x16x32_f16 v[62:65], v[176:179], v[192:195], v[62:65]
	ds_read_b128 v[104:107], v122
	v_mfma_f32_16x16x32_f16 v[58:61], v[176:179], v[196:199], v[58:61]
	ds_read_b128 v[108:111], v122 offset:2048
	v_mfma_f32_16x16x32_f16 v[54:57], v[176:179], v[200:203], v[54:57]
	ds_read_b128 v[112:115], v122 offset:4096
	v_mfma_f32_16x16x32_f16 v[50:53], v[176:179], v[204:207], v[50:53]
	ds_read_b128 v[116:119], v122 offset:6144
	v_mfma_f32_16x16x32_f16 v[46:49], v[180:183], v[192:195], v[46:49]
	ds_read_b128 v[144:147], v121
	v_mfma_f32_16x16x32_f16 v[42:45], v[180:183], v[196:199], v[42:45]
	ds_read_b128 v[148:151], v121 offset:2048
	v_mfma_f32_16x16x32_f16 v[38:41], v[180:183], v[200:203], v[38:41]
	ds_read_b128 v[152:155], v121 offset:4096
	v_mfma_f32_16x16x32_f16 v[34:37], v[180:183], v[204:207], v[34:37]
	ds_read_b128 v[156:159], v121 offset:6144
	v_mfma_f32_16x16x32_f16 v[30:33], v[184:187], v[192:195], v[30:33]
	ds_read_b128 v[160:163], v123
	v_mfma_f32_16x16x32_f16 v[26:29], v[184:187], v[196:199], v[26:29]
	ds_read_b128 v[164:167], v123 offset:2048
	v_mfma_f32_16x16x32_f16 v[22:25], v[184:187], v[200:203], v[22:25]
	ds_read_b128 v[168:171], v123 offset:4096
	v_mfma_f32_16x16x32_f16 v[18:21], v[184:187], v[204:207], v[18:21]
	ds_read_b128 v[172:175], v123 offset:6144
	v_mfma_f32_16x16x32_f16 v[14:17], v[188:191], v[192:195], v[14:17]
	v_mfma_f32_16x16x32_f16 v[10:13], v[188:191], v[196:199], v[10:13]
	s_mov_b32 m0, s49
	v_mfma_f32_16x16x32_f16 v[6:9], v[188:191], v[200:203], v[6:9]
	global_load_lds_dwordx4 v[76:77], off
	v_mfma_f32_16x16x32_f16 v[2:5], v[188:191], v[204:207], v[2:5]
	v_mfma_f32_16x16x32_f16 v[62:65], v[208:211], v[224:227], v[62:65]
	s_add_u32 m0, s49, 0x2000
	v_mfma_f32_16x16x32_f16 v[58:61], v[208:211], v[228:231], v[58:61]
	global_load_lds_dwordx4 v[74:75], off
	v_mfma_f32_16x16x32_f16 v[54:57], v[208:211], v[232:235], v[54:57]
	v_mfma_f32_16x16x32_f16 v[50:53], v[208:211], v[236:239], v[50:53]
	s_add_u32 m0, s49, 0x4000
	v_mfma_f32_16x16x32_f16 v[46:49], v[212:215], v[224:227], v[46:49]
	global_load_lds_dwordx4 v[70:71], off
	v_mfma_f32_16x16x32_f16 v[42:45], v[212:215], v[228:231], v[42:45]
	v_mfma_f32_16x16x32_f16 v[38:41], v[212:215], v[232:235], v[38:41]
	s_add_u32 m0, s49, 0x6000
	v_mfma_f32_16x16x32_f16 v[34:37], v[212:215], v[236:239], v[34:37]
	global_load_lds_dwordx4 v[68:69], off
	v_mfma_f32_16x16x32_f16 v[30:33], v[216:219], v[224:227], v[30:33]
	v_mfma_f32_16x16x32_f16 v[26:29], v[216:219], v[228:231], v[26:29]
	s_add_u32 m0, s49, 0x8000
	v_mfma_f32_16x16x32_f16 v[22:25], v[216:219], v[232:235], v[22:25]
	global_load_lds_dwordx4 v[72:73], off
	v_mfma_f32_16x16x32_f16 v[18:21], v[216:219], v[236:239], v[18:21]
	v_mfma_f32_16x16x32_f16 v[14:17], v[220:223], v[224:227], v[14:17]
	s_add_u32 m0, s49, 0xa000
	v_mfma_f32_16x16x32_f16 v[10:13], v[220:223], v[228:231], v[10:13]
	global_load_lds_dwordx4 v[66:67], off
	v_mfma_f32_16x16x32_f16 v[6:9], v[220:223], v[232:235], v[6:9]
	v_mfma_f32_16x16x32_f16 v[2:5], v[220:223], v[236:239], v[2:5]
	s_setprio 0
	v_lshl_add_u64 v[76:77], v[76:77], 0, s[0:1]
	v_lshl_add_u64 v[74:75], v[74:75], 0, s[0:1]
	v_lshl_add_u64 v[70:71], v[70:71], 0, s[0:1]
	v_lshl_add_u64 v[68:69], v[68:69], 0, s[0:1]
	v_lshl_add_u64 v[72:73], v[72:73], 0, s[0:1]
	v_lshl_add_u64 v[66:67], v[66:67], 0, s[0:1]
	s_add_i32 s48, s48, 1
	s_add_i32 s49, s45, 1
	s_cmp_lg_u32 s45, 2
	s_cselect_b32 s45, s49, 0
	s_add_i32 s49, s46, 1
	s_cmp_lg_u32 s46, 2
	s_cselect_b32 s46, s49, 0
	s_cmp_lt_u32 s48, 12
	s_cbranch_scc1 .LBB1_36
	s_waitcnt vmcnt(6)
	s_waitcnt lgkmcnt(0)
	s_barrier
	s_mul_i32 s49, s46, 0xc000
	s_add_u32 s50, s49, s3
	s_add_u32 s51, s49, s2
	v_add3_u32 v120, s50, v86, v85
	v_add3_u32 v121, s50, v86, v84
	v_add3_u32 v122, s51, v81, v85
	v_add3_u32 v123, s51, v81, v84
	s_mul_i32 s49, s45, 0xc000
	s_add_u32 s49, s49, s44
	s_setprio 1
	ds_read_b128 v[176:179], v120
	ds_read_b128 v[180:183], v120 offset:2048
	ds_read_b128 v[184:187], v120 offset:4096
	ds_read_b128 v[188:191], v120 offset:6144
	v_mfma_f32_16x16x32_f16 v[62:65], v[88:91], v[104:107], v[62:65]
	ds_read_b128 v[192:195], v122
	v_mfma_f32_16x16x32_f16 v[58:61], v[88:91], v[108:111], v[58:61]
	ds_read_b128 v[196:199], v122 offset:2048
	v_mfma_f32_16x16x32_f16 v[54:57], v[88:91], v[112:115], v[54:57]
	ds_read_b128 v[200:203], v122 offset:4096
	v_mfma_f32_16x16x32_f16 v[50:53], v[88:91], v[116:119], v[50:53]
	ds_read_b128 v[204:207], v122 offset:6144
	v_mfma_f32_16x16x32_f16 v[46:49], v[92:95], v[104:107], v[46:49]
	ds_read_b128 v[208:211], v121
	v_mfma_f32_16x16x32_f16 v[42:45], v[92:95], v[108:111], v[42:45]
	ds_read_b128 v[212:215], v121 offset:2048
	v_mfma_f32_16x16x32_f16 v[38:41], v[92:95], v[112:115], v[38:41]
	ds_read_b128 v[216:219], v121 offset:4096
	v_mfma_f32_16x16x32_f16 v[34:37], v[92:95], v[116:119], v[34:37]
	ds_read_b128 v[220:223], v121 offset:6144
	v_mfma_f32_16x16x32_f16 v[30:33], v[96:99], v[104:107], v[30:33]
	ds_read_b128 v[224:227], v123
	v_mfma_f32_16x16x32_f16 v[26:29], v[96:99], v[108:111], v[26:29]
	ds_read_b128 v[228:231], v123 offset:2048
	v_mfma_f32_16x16x32_f16 v[22:25], v[96:99], v[112:115], v[22:25]
	ds_read_b128 v[232:235], v123 offset:4096
	v_mfma_f32_16x16x32_f16 v[18:21], v[96:99], v[116:119], v[18:21]
	ds_read_b128 v[236:239], v123 offset:6144
	v_mfma_f32_16x16x32_f16 v[14:17], v[100:103], v[104:107], v[14:17]
	v_mfma_f32_16x16x32_f16 v[10:13], v[100:103], v[108:111], v[10:13]
	s_mov_b32 m0, s49
	v_mfma_f32_16x16x32_f16 v[6:9], v[100:103], v[112:115], v[6:9]
	global_load_lds_dwordx4 v[76:77], off
	v_mfma_f32_16x16x32_f16 v[2:5], v[100:103], v[116:119], v[2:5]
	v_mfma_f32_16x16x32_f16 v[62:65], v[144:147], v[160:163], v[62:65]
	s_add_u32 m0, s49, 0x2000
	v_mfma_f32_16x16x32_f16 v[58:61], v[144:147], v[164:167], v[58:61]
	global_load_lds_dwordx4 v[74:75], off
	v_mfma_f32_16x16x32_f16 v[54:57], v[144:147], v[168:171], v[54:57]
	v_mfma_f32_16x16x32_f16 v[50:53], v[144:147], v[172:175], v[50:53]
	s_add_u32 m0, s49, 0x4000
	v_mfma_f32_16x16x32_f16 v[46:49], v[148:151], v[160:163], v[46:49]
	global_load_lds_dwordx4 v[70:71], off
	v_mfma_f32_16x16x32_f16 v[42:45], v[148:151], v[164:167], v[42:45]
	v_mfma_f32_16x16x32_f16 v[38:41], v[148:151], v[168:171], v[38:41]
	s_add_u32 m0, s49, 0x6000
	v_mfma_f32_16x16x32_f16 v[34:37], v[148:151], v[172:175], v[34:37]
	global_load_lds_dwordx4 v[68:69], off
	v_mfma_f32_16x16x32_f16 v[30:33], v[152:155], v[160:163], v[30:33]
	v_mfma_f32_16x16x32_f16 v[26:29], v[152:155], v[164:167], v[26:29]
	s_add_u32 m0, s49, 0x8000
	v_mfma_f32_16x16x32_f16 v[22:25], v[152:155], v[168:171], v[22:25]
	global_load_lds_dwordx4 v[72:73], off
	v_mfma_f32_16x16x32_f16 v[18:21], v[152:155], v[172:175], v[18:21]
	v_mfma_f32_16x16x32_f16 v[14:17], v[156:159], v[160:163], v[14:17]
	s_add_u32 m0, s49, 0xa000
	v_mfma_f32_16x16x32_f16 v[10:13], v[156:159], v[164:167], v[10:13]
	global_load_lds_dwordx4 v[66:67], off
	v_mfma_f32_16x16x32_f16 v[6:9], v[156:159], v[168:171], v[6:9]
	v_mfma_f32_16x16x32_f16 v[2:5], v[156:159], v[172:175], v[2:5]
	s_setprio 0
	v_lshl_add_u64 v[76:77], v[76:77], 0, s[0:1]
	v_lshl_add_u64 v[74:75], v[74:75], 0, s[0:1]
	v_lshl_add_u64 v[70:71], v[70:71], 0, s[0:1]
	v_lshl_add_u64 v[68:69], v[68:69], 0, s[0:1]
	v_lshl_add_u64 v[72:73], v[72:73], 0, s[0:1]
	v_lshl_add_u64 v[66:67], v[66:67], 0, s[0:1]
	s_add_i32 s48, s48, 1
	s_add_i32 s49, s45, 1
	s_cmp_lg_u32 s45, 2
	s_cselect_b32 s45, s49, 0
	s_add_i32 s49, s46, 1
	s_cmp_lg_u32 s46, 2
	s_cselect_b32 s46, s49, 0
	s_waitcnt vmcnt(6)
	s_waitcnt lgkmcnt(0)
	s_barrier
	s_mul_i32 s49, s46, 0xc000
	s_add_u32 s50, s49, s3
	s_add_u32 s51, s49, s2
	v_add3_u32 v120, s50, v86, v85
	v_add3_u32 v121, s50, v86, v84
	v_add3_u32 v122, s51, v81, v85
	v_add3_u32 v123, s51, v81, v84
	s_setprio 1
	ds_read_b128 v[88:91], v120
	ds_read_b128 v[92:95], v120 offset:2048
	ds_read_b128 v[96:99], v120 offset:4096
	ds_read_b128 v[100:103], v120 offset:6144
	v_mfma_f32_16x16x32_f16 v[62:65], v[176:179], v[192:195], v[62:65]
	ds_read_b128 v[104:107], v122
	v_mfma_f32_16x16x32_f16 v[58:61], v[176:179], v[196:199], v[58:61]
	ds_read_b128 v[108:111], v122 offset:2048
	v_mfma_f32_16x16x32_f16 v[54:57], v[176:179], v[200:203], v[54:57]
	ds_read_b128 v[112:115], v122 offset:4096
	v_mfma_f32_16x16x32_f16 v[50:53], v[176:179], v[204:207], v[50:53]
	ds_read_b128 v[116:119], v122 offset:6144
	v_mfma_f32_16x16x32_f16 v[46:49], v[180:183], v[192:195], v[46:49]
	ds_read_b128 v[144:147], v121
	v_mfma_f32_16x16x32_f16 v[42:45], v[180:183], v[196:199], v[42:45]
	ds_read_b128 v[148:151], v121 offset:2048
	v_mfma_f32_16x16x32_f16 v[38:41], v[180:183], v[200:203], v[38:41]
	ds_read_b128 v[152:155], v121 offset:4096
	v_mfma_f32_16x16x32_f16 v[34:37], v[180:183], v[204:207], v[34:37]
	ds_read_b128 v[156:159], v121 offset:6144
	v_mfma_f32_16x16x32_f16 v[30:33], v[184:187], v[192:195], v[30:33]
	ds_read_b128 v[160:163], v123
	v_mfma_f32_16x16x32_f16 v[26:29], v[184:187], v[196:199], v[26:29]
	ds_read_b128 v[164:167], v123 offset:2048
	v_mfma_f32_16x16x32_f16 v[22:25], v[184:187], v[200:203], v[22:25]
	ds_read_b128 v[168:171], v123 offset:4096
	v_mfma_f32_16x16x32_f16 v[18:21], v[184:187], v[204:207], v[18:21]
	ds_read_b128 v[172:175], v123 offset:6144
	v_mfma_f32_16x16x32_f16 v[14:17], v[188:191], v[192:195], v[14:17]
	v_mfma_f32_16x16x32_f16 v[10:13], v[188:191], v[196:199], v[10:13]
	v_mfma_f32_16x16x32_f16 v[6:9], v[188:191], v[200:203], v[6:9]
	v_mfma_f32_16x16x32_f16 v[2:5], v[188:191], v[204:207], v[2:5]
	v_mfma_f32_16x16x32_f16 v[62:65], v[208:211], v[224:227], v[62:65]
	v_mfma_f32_16x16x32_f16 v[58:61], v[208:211], v[228:231], v[58:61]
	v_mfma_f32_16x16x32_f16 v[54:57], v[208:211], v[232:235], v[54:57]
	v_mfma_f32_16x16x32_f16 v[50:53], v[208:211], v[236:239], v[50:53]
	v_mfma_f32_16x16x32_f16 v[46:49], v[212:215], v[224:227], v[46:49]
	v_mfma_f32_16x16x32_f16 v[42:45], v[212:215], v[228:231], v[42:45]
	v_mfma_f32_16x16x32_f16 v[38:41], v[212:215], v[232:235], v[38:41]
	v_mfma_f32_16x16x32_f16 v[34:37], v[212:215], v[236:239], v[34:37]
	v_mfma_f32_16x16x32_f16 v[30:33], v[216:219], v[224:227], v[30:33]
	v_mfma_f32_16x16x32_f16 v[26:29], v[216:219], v[228:231], v[26:29]
	v_mfma_f32_16x16x32_f16 v[22:25], v[216:219], v[232:235], v[22:25]
	v_mfma_f32_16x16x32_f16 v[18:21], v[216:219], v[236:239], v[18:21]
	v_mfma_f32_16x16x32_f16 v[14:17], v[220:223], v[224:227], v[14:17]
	v_mfma_f32_16x16x32_f16 v[10:13], v[220:223], v[228:231], v[10:13]
	v_mfma_f32_16x16x32_f16 v[6:9], v[220:223], v[232:235], v[6:9]
	v_mfma_f32_16x16x32_f16 v[2:5], v[220:223], v[236:239], v[2:5]
	s_setprio 0
	s_add_i32 s48, s48, 1
	s_add_i32 s49, s45, 1
	s_cmp_lg_u32 s45, 2
	s_cselect_b32 s45, s49, 0
	s_add_i32 s49, s46, 1
	s_cmp_lg_u32 s46, 2
	s_cselect_b32 s46, s49, 0
	s_waitcnt vmcnt(0)
	s_waitcnt lgkmcnt(0)
	s_barrier
	s_mul_i32 s49, s46, 0xc000
	s_add_u32 s50, s49, s3
	s_add_u32 s51, s49, s2
	v_add3_u32 v120, s50, v86, v85
	v_add3_u32 v121, s50, v86, v84
	v_add3_u32 v122, s51, v81, v85
	v_add3_u32 v123, s51, v81, v84
	s_setprio 1
	ds_read_b128 v[176:179], v120
	ds_read_b128 v[180:183], v120 offset:2048
	ds_read_b128 v[184:187], v120 offset:4096
	ds_read_b128 v[188:191], v120 offset:6144
	v_mfma_f32_16x16x32_f16 v[62:65], v[88:91], v[104:107], v[62:65]
	ds_read_b128 v[192:195], v122
	v_mfma_f32_16x16x32_f16 v[58:61], v[88:91], v[108:111], v[58:61]
	ds_read_b128 v[196:199], v122 offset:2048
	v_mfma_f32_16x16x32_f16 v[54:57], v[88:91], v[112:115], v[54:57]
	ds_read_b128 v[200:203], v122 offset:4096
	v_mfma_f32_16x16x32_f16 v[50:53], v[88:91], v[116:119], v[50:53]
	ds_read_b128 v[204:207], v122 offset:6144
	v_mfma_f32_16x16x32_f16 v[46:49], v[92:95], v[104:107], v[46:49]
	ds_read_b128 v[208:211], v121
	v_mfma_f32_16x16x32_f16 v[42:45], v[92:95], v[108:111], v[42:45]
	ds_read_b128 v[212:215], v121 offset:2048
	v_mfma_f32_16x16x32_f16 v[38:41], v[92:95], v[112:115], v[38:41]
	ds_read_b128 v[216:219], v121 offset:4096
	v_mfma_f32_16x16x32_f16 v[34:37], v[92:95], v[116:119], v[34:37]
	ds_read_b128 v[220:223], v121 offset:6144
	v_mfma_f32_16x16x32_f16 v[30:33], v[96:99], v[104:107], v[30:33]
	ds_read_b128 v[224:227], v123
	v_mfma_f32_16x16x32_f16 v[26:29], v[96:99], v[108:111], v[26:29]
	ds_read_b128 v[228:231], v123 offset:2048
	v_mfma_f32_16x16x32_f16 v[22:25], v[96:99], v[112:115], v[22:25]
	ds_read_b128 v[232:235], v123 offset:4096
	v_mfma_f32_16x16x32_f16 v[18:21], v[96:99], v[116:119], v[18:21]
	ds_read_b128 v[236:239], v123 offset:6144
	v_mfma_f32_16x16x32_f16 v[14:17], v[100:103], v[104:107], v[14:17]
	v_mfma_f32_16x16x32_f16 v[10:13], v[100:103], v[108:111], v[10:13]
	v_mfma_f32_16x16x32_f16 v[6:9], v[100:103], v[112:115], v[6:9]
	v_mfma_f32_16x16x32_f16 v[2:5], v[100:103], v[116:119], v[2:5]
	v_mfma_f32_16x16x32_f16 v[62:65], v[144:147], v[160:163], v[62:65]
	v_mfma_f32_16x16x32_f16 v[58:61], v[144:147], v[164:167], v[58:61]
	v_mfma_f32_16x16x32_f16 v[54:57], v[144:147], v[168:171], v[54:57]
	v_mfma_f32_16x16x32_f16 v[50:53], v[144:147], v[172:175], v[50:53]
	v_mfma_f32_16x16x32_f16 v[46:49], v[148:151], v[160:163], v[46:49]
	v_mfma_f32_16x16x32_f16 v[42:45], v[148:151], v[164:167], v[42:45]
	v_mfma_f32_16x16x32_f16 v[38:41], v[148:151], v[168:171], v[38:41]
	v_mfma_f32_16x16x32_f16 v[34:37], v[148:151], v[172:175], v[34:37]
	v_mfma_f32_16x16x32_f16 v[30:33], v[152:155], v[160:163], v[30:33]
	v_mfma_f32_16x16x32_f16 v[26:29], v[152:155], v[164:167], v[26:29]
	v_mfma_f32_16x16x32_f16 v[22:25], v[152:155], v[168:171], v[22:25]
	v_mfma_f32_16x16x32_f16 v[18:21], v[152:155], v[172:175], v[18:21]
	v_mfma_f32_16x16x32_f16 v[14:17], v[156:159], v[160:163], v[14:17]
	v_mfma_f32_16x16x32_f16 v[10:13], v[156:159], v[164:167], v[10:13]
	v_mfma_f32_16x16x32_f16 v[6:9], v[156:159], v[168:171], v[6:9]
	v_mfma_f32_16x16x32_f16 v[2:5], v[156:159], v[172:175], v[2:5]
	s_setprio 0
	s_add_i32 s48, s48, 1
	s_add_i32 s49, s45, 1
	s_cmp_lg_u32 s45, 2
	s_cselect_b32 s45, s49, 0
	s_add_i32 s49, s46, 1
	s_cmp_lg_u32 s46, 2
	s_cselect_b32 s46, s49, 0
	s_waitcnt lgkmcnt(0)
	s_setprio 1
	v_mfma_f32_16x16x32_f16 v[62:65], v[176:179], v[192:195], v[62:65]
	v_mfma_f32_16x16x32_f16 v[58:61], v[176:179], v[196:199], v[58:61]
	v_mfma_f32_16x16x32_f16 v[54:57], v[176:179], v[200:203], v[54:57]
	v_mfma_f32_16x16x32_f16 v[50:53], v[176:179], v[204:207], v[50:53]
	v_mfma_f32_16x16x32_f16 v[46:49], v[180:183], v[192:195], v[46:49]
	v_mfma_f32_16x16x32_f16 v[42:45], v[180:183], v[196:199], v[42:45]
	v_mfma_f32_16x16x32_f16 v[38:41], v[180:183], v[200:203], v[38:41]
	v_mfma_f32_16x16x32_f16 v[34:37], v[180:183], v[204:207], v[34:37]
	v_mfma_f32_16x16x32_f16 v[30:33], v[184:187], v[192:195], v[30:33]
	v_mfma_f32_16x16x32_f16 v[26:29], v[184:187], v[196:199], v[26:29]
	v_mfma_f32_16x16x32_f16 v[22:25], v[184:187], v[200:203], v[22:25]
	v_mfma_f32_16x16x32_f16 v[18:21], v[184:187], v[204:207], v[18:21]
	v_mfma_f32_16x16x32_f16 v[14:17], v[188:191], v[192:195], v[14:17]
	v_mfma_f32_16x16x32_f16 v[10:13], v[188:191], v[196:199], v[10:13]
	v_mfma_f32_16x16x32_f16 v[6:9], v[188:191], v[200:203], v[6:9]
	v_mfma_f32_16x16x32_f16 v[2:5], v[188:191], v[204:207], v[2:5]
	v_mfma_f32_16x16x32_f16 v[62:65], v[208:211], v[224:227], v[62:65]
	v_mfma_f32_16x16x32_f16 v[58:61], v[208:211], v[228:231], v[58:61]
	v_mfma_f32_16x16x32_f16 v[54:57], v[208:211], v[232:235], v[54:57]
	v_mfma_f32_16x16x32_f16 v[50:53], v[208:211], v[236:239], v[50:53]
	v_mfma_f32_16x16x32_f16 v[46:49], v[212:215], v[224:227], v[46:49]
	v_mfma_f32_16x16x32_f16 v[42:45], v[212:215], v[228:231], v[42:45]
	v_mfma_f32_16x16x32_f16 v[38:41], v[212:215], v[232:235], v[38:41]
	v_mfma_f32_16x16x32_f16 v[34:37], v[212:215], v[236:239], v[34:37]
	v_mfma_f32_16x16x32_f16 v[30:33], v[216:219], v[224:227], v[30:33]
	v_mfma_f32_16x16x32_f16 v[26:29], v[216:219], v[228:231], v[26:29]
	v_mfma_f32_16x16x32_f16 v[22:25], v[216:219], v[232:235], v[22:25]
	v_mfma_f32_16x16x32_f16 v[18:21], v[216:219], v[236:239], v[18:21]
	v_mfma_f32_16x16x32_f16 v[14:17], v[220:223], v[224:227], v[14:17]
	v_mfma_f32_16x16x32_f16 v[10:13], v[220:223], v[228:231], v[10:13]
	v_mfma_f32_16x16x32_f16 v[6:9], v[220:223], v[232:235], v[6:9]
	v_mfma_f32_16x16x32_f16 v[2:5], v[220:223], v[236:239], v[2:5]
	s_setprio 0
	s_branch .Lqk_epi_start
